# adds P4 router-bias load hoisted out of the group loop (kept in a VGPR) with vmcnt(9) so the group no longer drains its int8/hs stores; on top of swiglu+P7+census
# speedup vs baseline: 1.0113x; 1.0011x over previous
; __device__ __forceinline__ unsigned pk2(float lo, float hi) { const f32x2_t v = {lo, hi}; const bf16x2_t b = __builtin_convertvector(v, bf16x2_t); return __builtin_bit_cast(unsigned, b); }
; __device__ __forceinline__ unsigned f2bf(float f) { return pk2(f, f) & 0xffffu; }
; __device__ __forceinline__ void p4_ln_router(Frame& F, int l) {
;     ...
;     bf16x8_t whi[4][2], wlo[4][2];
; #pragma unroll
;     for (int ks = 0; ks < 4; ++ks)
; #pragma unroll
;         for (int nt = 0; nt < 2; ++nt) { float w[8], wl[8];
; #pragma unroll
;             for (int j = 0; j < 8; ++j) { w[j] = Wr[(size_t)(128 * wave + 32 * ks + 8 * q4 + j) * NEXP + 16 * nt + li]; wl[j] = w[j] - bf2f((unsigned short)f2bf(w[j])); }
;             v4u a, b; a.x = pk2(w[0], w[1]); a.y = pk2(w[2], w[3]); a.z = pk2(w[4], w[5]); a.w = pk2(w[6], w[7]); b.x = pk2(wl[0], wl[1]); b.y = pk2(wl[2], wl[3]); b.z = pk2(wl[4], wl[5]); b.w = pk2(wl[6], wl[7]);
;             whi[ks][nt] = __builtin_bit_cast(bf16x8_t, a); wlo[ks][nt] = __builtin_bit_cast(bf16x8_t, b); }
.LBB0_633:
	s_or_b64 exec, exec, s[4:5]
	s_waitcnt lgkmcnt(0)
	v_mov_b32_e32 v0, s40
	v_mov_b32_e32 v1, s41
	s_barrier
	v_mov_b32_e32 v73, s27
	v_readfirstlane_b32 s4, v0
	v_readfirstlane_b32 s5, v1
	v_mov_b32_e32 v76, s29
	v_mov_b32_e32 v77, s17
	v_mov_b32_e32 v78, s25
	v_mov_b32_e32 v72, v179
	s_load_dwordx8 s[36:43], s[4:5], 0x58
	v_readlane_b32 s10, v255, 8
	s_lshl_b32 s92, s10, 15
	s_lshl_b64 s[56:57], s[92:93], 2
	v_bfe_u32 v66, v72, 4, 2
	v_readlane_b32 s12, v253, 44
	s_waitcnt lgkmcnt(0)
	s_add_u32 s10, s40, s56
	v_and_b32_e32 v67, 15, v72
	v_lshl_or_b32 v2, v66, 3, s12
	s_addc_u32 s11, s41, s57
	v_lshlrev_b32_e32 v168, 2, v67
	v_mov_b32_e32 v3, v169
	v_or_b32_e32 v10, 3, v2
	v_mov_b32_e32 v11, v169
	v_or_b32_e32 v18, 7, v2
	v_mov_b32_e32 v19, v169
	v_lshl_add_u64 v[0:1], s[10:11], 0, v[168:169]
	v_lshlrev_b64 v[4:5], 7, v[2:3]
	s_waitcnt vmcnt(0)
	v_or_b32_e32 v6, 1, v2
	v_mov_b32_e32 v7, v169
	v_or_b32_e32 v8, 2, v2
	v_mov_b32_e32 v9, v169
	v_lshlrev_b64 v[10:11], 7, v[10:11]
	v_or_b32_e32 v12, 4, v2
	v_mov_b32_e32 v13, v169
	v_or_b32_e32 v14, 5, v2
	v_mov_b32_e32 v15, v169
	v_or_b32_e32 v16, 6, v2
	v_mov_b32_e32 v17, v169
	v_lshlrev_b64 v[18:19], 7, v[18:19]
	v_lshl_add_u64 v[4:5], v[0:1], 0, v[4:5]
	v_lshlrev_b64 v[6:7], 7, v[6:7]
	v_lshlrev_b64 v[8:9], 7, v[8:9]
	v_lshl_add_u64 v[10:11], v[0:1], 0, v[10:11]
	v_lshlrev_b64 v[12:13], 7, v[12:13]
	v_lshlrev_b64 v[14:15], 7, v[14:15]
	v_lshlrev_b64 v[16:17], 7, v[16:17]
	v_lshl_add_u64 v[18:19], v[0:1], 0, v[18:19]
	v_lshl_add_u64 v[6:7], v[0:1], 0, v[6:7]
	v_lshl_add_u64 v[8:9], v[0:1], 0, v[8:9]
	v_lshl_add_u64 v[12:13], v[0:1], 0, v[12:13]
	v_lshl_add_u64 v[14:15], v[0:1], 0, v[14:15]
	v_lshl_add_u64 v[16:17], v[0:1], 0, v[16:17]
	global_load_dword v60, v[4:5], off
	global_load_dword v61, v[6:7], off
	global_load_dword v58, v[8:9], off
	global_load_dword v59, v[10:11], off
	global_load_dword v51, v[10:11], off offset:64
	global_load_dword v50, v[8:9], off offset:64
	global_load_dword v53, v[6:7], off offset:64
	global_load_dword v52, v[4:5], off offset:64
	global_load_dword v62, v[12:13], off
	global_load_dword v63, v[14:15], off
	global_load_dword v64, v[16:17], off
	global_load_dword v65, v[18:19], off
	global_load_dword v57, v[18:19], off offset:64
	global_load_dword v56, v[16:17], off offset:64
	global_load_dword v55, v[14:15], off offset:64
	global_load_dword v54, v[12:13], off offset:64
	v_or_b32_e32 v4, 32, v2
	v_mov_b32_e32 v5, v169
	v_or_b32_e32 v10, 35, v2
	v_mov_b32_e32 v11, v169
	v_or_b32_e32 v18, 39, v2
	v_mov_b32_e32 v19, v169
	v_lshlrev_b64 v[4:5], 7, v[4:5]
	v_or_b32_e32 v6, 33, v2
	v_mov_b32_e32 v7, v169
	v_or_b32_e32 v8, 34, v2
	v_mov_b32_e32 v9, v169
	v_lshlrev_b64 v[10:11], 7, v[10:11]
	v_or_b32_e32 v12, 36, v2
	v_mov_b32_e32 v13, v169
	v_or_b32_e32 v14, 37, v2
	v_mov_b32_e32 v15, v169
	v_or_b32_e32 v16, 38, v2
	v_mov_b32_e32 v17, v169
	v_lshlrev_b64 v[18:19], 7, v[18:19]
	v_lshl_add_u64 v[4:5], v[0:1], 0, v[4:5]
	v_lshlrev_b64 v[6:7], 7, v[6:7]
	v_lshlrev_b64 v[8:9], 7, v[8:9]
	v_lshl_add_u64 v[10:11], v[0:1], 0, v[10:11]
	v_lshlrev_b64 v[12:13], 7, v[12:13]
	v_lshlrev_b64 v[14:15], 7, v[14:15]
	v_lshlrev_b64 v[16:17], 7, v[16:17]
	v_lshl_add_u64 v[18:19], v[0:1], 0, v[18:19]
	v_lshl_add_u64 v[6:7], v[0:1], 0, v[6:7]
	v_lshl_add_u64 v[8:9], v[0:1], 0, v[8:9]
	v_lshl_add_u64 v[12:13], v[0:1], 0, v[12:13]
	v_lshl_add_u64 v[14:15], v[0:1], 0, v[14:15]
	v_lshl_add_u64 v[16:17], v[0:1], 0, v[16:17]
	global_load_dword v44, v[4:5], off
	global_load_dword v45, v[6:7], off
	global_load_dword v42, v[8:9], off
	global_load_dword v43, v[10:11], off
	global_load_dword v35, v[10:11], off offset:64
	global_load_dword v34, v[8:9], off offset:64
	global_load_dword v37, v[6:7], off offset:64
	global_load_dword v36, v[4:5], off offset:64
	global_load_dword v46, v[12:13], off
	global_load_dword v47, v[14:15], off
	global_load_dword v48, v[16:17], off
	global_load_dword v49, v[18:19], off
	global_load_dword v41, v[18:19], off offset:64
	global_load_dword v40, v[16:17], off offset:64
	global_load_dword v39, v[14:15], off offset:64
	global_load_dword v38, v[12:13], off offset:64
	v_or_b32_e32 v4, 64, v2
	v_mov_b32_e32 v5, v169
	v_or_b32_e32 v10, 0x43, v2
	v_mov_b32_e32 v11, v169
	v_or_b32_e32 v18, 0x47, v2
	v_mov_b32_e32 v19, v169
	v_lshlrev_b64 v[4:5], 7, v[4:5]
	v_or_b32_e32 v6, 0x41, v2
	v_mov_b32_e32 v7, v169
	v_or_b32_e32 v8, 0x42, v2
	v_mov_b32_e32 v9, v169
	v_lshlrev_b64 v[10:11], 7, v[10:11]
	v_or_b32_e32 v12, 0x44, v2
	v_mov_b32_e32 v13, v169
	v_or_b32_e32 v14, 0x45, v2
	v_mov_b32_e32 v15, v169
	v_or_b32_e32 v16, 0x46, v2
	v_mov_b32_e32 v17, v169
	v_lshlrev_b64 v[18:19], 7, v[18:19]
	v_lshl_add_u64 v[4:5], v[0:1], 0, v[4:5]
	v_lshlrev_b64 v[6:7], 7, v[6:7]
	v_lshlrev_b64 v[8:9], 7, v[8:9]
	v_lshl_add_u64 v[10:11], v[0:1], 0, v[10:11]
	v_lshlrev_b64 v[12:13], 7, v[12:13]
	v_lshlrev_b64 v[14:15], 7, v[14:15]
	v_lshlrev_b64 v[16:17], 7, v[16:17]
	v_lshl_add_u64 v[22:23], v[0:1], 0, v[18:19]
	v_lshl_add_u64 v[6:7], v[0:1], 0, v[6:7]
	v_lshl_add_u64 v[8:9], v[0:1], 0, v[8:9]
	v_lshl_add_u64 v[12:13], v[0:1], 0, v[12:13]
	v_lshl_add_u64 v[14:15], v[0:1], 0, v[14:15]
	v_lshl_add_u64 v[16:17], v[0:1], 0, v[16:17]
	global_load_dword v28, v[4:5], off
	global_load_dword v29, v[6:7], off
	global_load_dword v26, v[8:9], off
	global_load_dword v27, v[10:11], off
	global_load_dword v19, v[10:11], off offset:64
	global_load_dword v18, v[8:9], off offset:64
	global_load_dword v21, v[6:7], off offset:64
	global_load_dword v20, v[4:5], off offset:64
	global_load_dword v30, v[12:13], off
	global_load_dword v31, v[14:15], off
	global_load_dword v32, v[16:17], off
	global_load_dword v33, v[22:23], off
; __device__ __forceinline__ unsigned pk2(float lo, float hi) { const f32x2_t v = {lo, hi}; const bf16x2_t b = __builtin_convertvector(v, bf16x2_t); return __builtin_bit_cast(unsigned, b); }
; __device__ __forceinline__ unsigned f2bf(float f) { return pk2(f, f) & 0xffffu; }
; __device__ __forceinline__ void p4_ln_router(Frame& F, int l) {
;     ...
;         for (int nt = 0; nt < 2; ++nt) { float w[8], wl[8];
; #pragma unroll
;             for (int j = 0; j < 8; ++j) { w[j] = Wr[(size_t)(128 * wave + 32 * ks + 8 * q4 + j) * NEXP + 16 * nt + li]; wl[j] = w[j] - bf2f((unsigned short)f2bf(w[j])); }
;             v4u a, b; a.x = pk2(w[0], w[1]); a.y = pk2(w[2], w[3]); a.z = pk2(w[4], w[5]); a.w = pk2(w[6], w[7]); b.x = pk2(wl[0], wl[1]); b.y = pk2(wl[2], wl[3]); b.z = pk2(wl[4], wl[5]); b.w = pk2(wl[6], wl[7]);
;             whi[ks][nt] = __builtin_bit_cast(bf16x8_t, a); wlo[ks][nt] = __builtin_bit_cast(bf16x8_t, b); }
;     __syncthreads();
	global_load_dword v25, v[22:23], off offset:64
	global_load_dword v24, v[16:17], off offset:64
	s_nop 0
	global_load_dword v23, v[14:15], off offset:64
	global_load_dword v22, v[12:13], off offset:64
	v_or_b32_e32 v10, 0x63, v2
	v_mov_b32_e32 v11, v169
	v_lshlrev_b64 v[10:11], 7, v[10:11]
	v_lshl_add_u64 v[14:15], v[0:1], 0, v[10:11]
	v_or_b32_e32 v10, 0x64, v2
	v_mov_b32_e32 v11, v169
	v_or_b32_e32 v4, 0x60, v2
	v_mov_b32_e32 v5, v169
	v_lshlrev_b64 v[10:11], 7, v[10:11]
	v_lshlrev_b64 v[4:5], 7, v[4:5]
	v_lshl_add_u64 v[68:69], v[0:1], 0, v[10:11]
	v_or_b32_e32 v10, 0x65, v2
	v_mov_b32_e32 v11, v169
	v_lshl_add_u64 v[6:7], v[0:1], 0, v[4:5]
	v_or_b32_e32 v4, 0x61, v2
	v_mov_b32_e32 v5, v169
	v_or_b32_e32 v8, 0x62, v2
	v_mov_b32_e32 v9, v169
	v_lshlrev_b64 v[10:11], 7, v[10:11]
	v_lshlrev_b64 v[4:5], 7, v[4:5]
	v_lshlrev_b64 v[8:9], 7, v[8:9]
	v_lshl_add_u64 v[70:71], v[0:1], 0, v[10:11]
	v_or_b32_e32 v10, 0x66, v2
	v_mov_b32_e32 v11, v169
	v_or_b32_e32 v2, 0x67, v2
	v_lshl_add_u64 v[4:5], v[0:1], 0, v[4:5]
	v_lshl_add_u64 v[8:9], v[0:1], 0, v[8:9]
	v_lshlrev_b64 v[10:11], 7, v[10:11]
	v_lshlrev_b64 v[2:3], 7, v[2:3]
	v_lshl_add_u64 v[74:75], v[0:1], 0, v[10:11]
	v_lshl_add_u64 v[0:1], v[0:1], 0, v[2:3]
	global_load_dword v12, v[6:7], off
	global_load_dword v13, v[4:5], off
	global_load_dword v10, v[8:9], off
	global_load_dword v11, v[14:15], off
	global_load_dword v3, v[14:15], off offset:64
	global_load_dword v2, v[8:9], off offset:64
	s_nop 0
	global_load_dword v5, v[4:5], off offset:64
	s_nop 0
	global_load_dword v4, v[6:7], off offset:64
	global_load_dword v14, v[68:69], off
	global_load_dword v15, v[70:71], off
	global_load_dword v16, v[74:75], off
	global_load_dword v17, v[0:1], off
	global_load_dword v9, v[0:1], off offset:64
	global_load_dword v8, v[74:75], off offset:64
	global_load_dword v7, v[70:71], off offset:64
	global_load_dword v6, v[68:69], off offset:64
	v_readlane_b32 s10, v253, 19
	v_readlane_b32 s11, v253, 20
	v_readfirstlane_b32 s14, v73
	v_readfirstlane_b32 s15, v76
	v_readfirstlane_b32 s17, v77
	v_readfirstlane_b32 s25, v78
	s_andn2_b64 vcc, exec, s[10:11]
	s_waitcnt vmcnt(63) expcnt(7) lgkmcnt(15)
	s_barrier
	s_cbranch_vccnz .LBB0_657
	s_waitcnt vmcnt(8)
	v_cvt_pk_bf16_f32 v0, v4, v5
	v_and_b32_e32 v69, 0xffff0000, v0
	v_lshlrev_b32_e32 v68, 16, v0
	v_cvt_pk_bf16_f32 v1, v2, v3
	v_pk_add_f32 v[4:5], v[4:5], v[68:69] neg_lo:[0,1] neg_hi:[0,1]
	v_and_b32_e32 v69, 0xffff0000, v1
	v_lshlrev_b32_e32 v68, 16, v1
	v_pk_add_f32 v[2:3], v[2:3], v[68:69] neg_lo:[0,1] neg_hi:[0,1]
	v_cvt_pk_bf16_f32 v4, v4, v5
	v_cvt_pk_bf16_f32 v5, v2, v3
	s_waitcnt vmcnt(0)
	v_cvt_pk_bf16_f32 v2, v6, v7
	v_and_b32_e32 v69, 0xffff0000, v2
	v_lshlrev_b32_e32 v68, 16, v2
	v_cvt_pk_bf16_f32 v3, v8, v9
	v_pk_add_f32 v[6:7], v[6:7], v[68:69] neg_lo:[0,1] neg_hi:[0,1]
	v_and_b32_e32 v69, 0xffff0000, v3
	v_lshlrev_b32_e32 v68, 16, v3
	v_pk_add_f32 v[8:9], v[8:9], v[68:69] neg_lo:[0,1] neg_hi:[0,1]
	v_cvt_pk_bf16_f32 v6, v6, v7
	v_cvt_pk_bf16_f32 v7, v8, v9
	v_cvt_pk_bf16_f32 v8, v12, v13
	v_and_b32_e32 v69, 0xffff0000, v8
	v_lshlrev_b32_e32 v68, 16, v8
	v_cvt_pk_bf16_f32 v9, v10, v11
	v_pk_add_f32 v[12:13], v[12:13], v[68:69] neg_lo:[0,1] neg_hi:[0,1]
	v_and_b32_e32 v69, 0xffff0000, v9
	v_lshlrev_b32_e32 v68, 16, v9
	v_pk_add_f32 v[10:11], v[10:11], v[68:69] neg_lo:[0,1] neg_hi:[0,1]
	v_cvt_pk_bf16_f32 v12, v12, v13
	v_cvt_pk_bf16_f32 v13, v10, v11
	v_cvt_pk_bf16_f32 v10, v14, v15
	v_and_b32_e32 v69, 0xffff0000, v10
	v_lshlrev_b32_e32 v68, 16, v10
	v_cvt_pk_bf16_f32 v11, v16, v17
	v_pk_add_f32 v[14:15], v[14:15], v[68:69] neg_lo:[0,1] neg_hi:[0,1]
	v_and_b32_e32 v69, 0xffff0000, v11
	v_lshlrev_b32_e32 v68, 16, v11
	v_pk_add_f32 v[16:17], v[16:17], v[68:69] neg_lo:[0,1] neg_hi:[0,1]
	v_cvt_pk_bf16_f32 v14, v14, v15
	v_cvt_pk_bf16_f32 v15, v16, v17
	v_cvt_pk_bf16_f32 v16, v20, v21
	v_and_b32_e32 v69, 0xffff0000, v16
	v_lshlrev_b32_e32 v68, 16, v16
	v_cvt_pk_bf16_f32 v17, v18, v19
	v_pk_add_f32 v[20:21], v[20:21], v[68:69] neg_lo:[0,1] neg_hi:[0,1]
	v_and_b32_e32 v69, 0xffff0000, v17
	v_lshlrev_b32_e32 v68, 16, v17
	v_pk_add_f32 v[18:19], v[18:19], v[68:69] neg_lo:[0,1] neg_hi:[0,1]
	v_cvt_pk_bf16_f32 v20, v20, v21
	v_cvt_pk_bf16_f32 v21, v18, v19
	v_cvt_pk_bf16_f32 v18, v22, v23
	v_and_b32_e32 v69, 0xffff0000, v18
	v_lshlrev_b32_e32 v68, 16, v18
	v_cvt_pk_bf16_f32 v19, v24, v25
	v_pk_add_f32 v[22:23], v[22:23], v[68:69] neg_lo:[0,1] neg_hi:[0,1]
	v_and_b32_e32 v69, 0xffff0000, v19
	v_lshlrev_b32_e32 v68, 16, v19
	v_pk_add_f32 v[24:25], v[24:25], v[68:69] neg_lo:[0,1] neg_hi:[0,1]
	v_cvt_pk_bf16_f32 v22, v22, v23
	v_cvt_pk_bf16_f32 v23, v24, v25
	v_cvt_pk_bf16_f32 v24, v28, v29
	v_and_b32_e32 v69, 0xffff0000, v24
	v_lshlrev_b32_e32 v68, 16, v24
	v_cvt_pk_bf16_f32 v25, v26, v27
	v_pk_add_f32 v[28:29], v[28:29], v[68:69] neg_lo:[0,1] neg_hi:[0,1]
	v_and_b32_e32 v69, 0xffff0000, v25
	v_lshlrev_b32_e32 v68, 16, v25
	v_pk_add_f32 v[26:27], v[26:27], v[68:69] neg_lo:[0,1] neg_hi:[0,1]
	v_cvt_pk_bf16_f32 v28, v28, v29
	v_cvt_pk_bf16_f32 v29, v26, v27
	v_cvt_pk_bf16_f32 v26, v30, v31
	v_and_b32_e32 v69, 0xffff0000, v26
	v_lshlrev_b32_e32 v68, 16, v26
	v_cvt_pk_bf16_f32 v27, v32, v33
	v_pk_add_f32 v[30:31], v[30:31], v[68:69] neg_lo:[0,1] neg_hi:[0,1]
	v_and_b32_e32 v69, 0xffff0000, v27
	v_lshlrev_b32_e32 v68, 16, v27
	v_pk_add_f32 v[32:33], v[32:33], v[68:69] neg_lo:[0,1] neg_hi:[0,1]
	v_cvt_pk_bf16_f32 v30, v30, v31
	v_cvt_pk_bf16_f32 v31, v32, v33
	v_cvt_pk_bf16_f32 v32, v36, v37
	v_and_b32_e32 v69, 0xffff0000, v32
	v_lshlrev_b32_e32 v68, 16, v32
	v_cvt_pk_bf16_f32 v33, v34, v35
	v_pk_add_f32 v[36:37], v[36:37], v[68:69] neg_lo:[0,1] neg_hi:[0,1]
; __device__ __forceinline__ unsigned pk2(float lo, float hi) { const f32x2_t v = {lo, hi}; const bf16x2_t b = __builtin_convertvector(v, bf16x2_t); return __builtin_bit_cast(unsigned, b); }
; __device__ __forceinline__ unsigned f2bf(float f) { return pk2(f, f) & 0xffffu; }
; __device__ __forceinline__ void p4_ln_router(Frame& F, int l) {
;     ...
;         for (int nt = 0; nt < 2; ++nt) { float w[8], wl[8];
; #pragma unroll
;             for (int j = 0; j < 8; ++j) { w[j] = Wr[(size_t)(128 * wave + 32 * ks + 8 * q4 + j) * NEXP + 16 * nt + li]; wl[j] = w[j] - bf2f((unsigned short)f2bf(w[j])); }
;             v4u a, b; a.x = pk2(w[0], w[1]); a.y = pk2(w[2], w[3]); a.z = pk2(w[4], w[5]); a.w = pk2(w[6], w[7]); b.x = pk2(wl[0], wl[1]); b.y = pk2(wl[2], wl[3]); b.z = pk2(wl[4], wl[5]); b.w = pk2(wl[6], wl[7]);
;             whi[ks][nt] = __builtin_bit_cast(bf16x8_t, a); wlo[ks][nt] = __builtin_bit_cast(bf16x8_t, b); }
;     __syncthreads();
;     for (int tb = F.vcu; tb < M / 256; tb += F.G) {
;         if (tid < 32) lcnt[tid] = 0;
;         v2u hA[2][4], mA[2][4], hB[2][4], mB[2][4];
; #pragma unroll
;         for (int r = 0; r < 2; ++r) { const size_t m0 = (size_t)(tb * 256 + 2 * wave + r); load_raw_q(hA[r], mA[r], HQ + m0 * D, HS + m0, MIX + m0 * D, lane);
;             load_raw_q(hB[r], mB[r], HQ + (m0 + 16) * D, HS + m0 + 16, MIX + (m0 + 16) * D, lane); }
;     ...
;             { const int row = tid >> 5, e = tid & 31; float val = br[e]; float pw[8];
	v_and_b32_e32 v69, 0xffff0000, v33
	v_lshlrev_b32_e32 v68, 16, v33
	v_pk_add_f32 v[34:35], v[34:35], v[68:69] neg_lo:[0,1] neg_hi:[0,1]
	v_cvt_pk_bf16_f32 v36, v36, v37
	v_cvt_pk_bf16_f32 v37, v34, v35
	v_cvt_pk_bf16_f32 v34, v38, v39
	v_and_b32_e32 v69, 0xffff0000, v34
	v_lshlrev_b32_e32 v68, 16, v34
	v_cvt_pk_bf16_f32 v35, v40, v41
	v_pk_add_f32 v[38:39], v[38:39], v[68:69] neg_lo:[0,1] neg_hi:[0,1]
	v_and_b32_e32 v69, 0xffff0000, v35
	v_lshlrev_b32_e32 v68, 16, v35
	v_pk_add_f32 v[40:41], v[40:41], v[68:69] neg_lo:[0,1] neg_hi:[0,1]
	v_cvt_pk_bf16_f32 v38, v38, v39
	v_cvt_pk_bf16_f32 v39, v40, v41
	v_cvt_pk_bf16_f32 v40, v44, v45
	v_and_b32_e32 v69, 0xffff0000, v40
	v_lshlrev_b32_e32 v68, 16, v40
	v_cvt_pk_bf16_f32 v41, v42, v43
	v_pk_add_f32 v[44:45], v[44:45], v[68:69] neg_lo:[0,1] neg_hi:[0,1]
	v_and_b32_e32 v69, 0xffff0000, v41
	v_lshlrev_b32_e32 v68, 16, v41
	v_pk_add_f32 v[42:43], v[42:43], v[68:69] neg_lo:[0,1] neg_hi:[0,1]
	v_cvt_pk_bf16_f32 v44, v44, v45
	v_cvt_pk_bf16_f32 v45, v42, v43
	v_cvt_pk_bf16_f32 v42, v46, v47
	v_and_b32_e32 v69, 0xffff0000, v42
	v_lshlrev_b32_e32 v68, 16, v42
	v_cvt_pk_bf16_f32 v43, v48, v49
	v_pk_add_f32 v[46:47], v[46:47], v[68:69] neg_lo:[0,1] neg_hi:[0,1]
	v_and_b32_e32 v69, 0xffff0000, v43
	v_lshlrev_b32_e32 v68, 16, v43
	s_add_u32 s10, s14, 0x19400000
	v_pk_add_f32 v[48:49], v[48:49], v[68:69] neg_lo:[0,1] neg_hi:[0,1]
	s_addc_u32 s11, s15, 0
	v_cvt_pk_bf16_f32 v46, v46, v47
	v_cvt_pk_bf16_f32 v47, v48, v49
	v_cvt_pk_bf16_f32 v48, v52, v53
	s_add_u32 s27, s14, 0x1d400000
	v_and_b32_e32 v69, 0xffff0000, v48
	v_lshlrev_b32_e32 v68, 16, v48
	v_cvt_pk_bf16_f32 v49, v50, v51
	s_addc_u32 s29, s15, 0
	v_pk_add_f32 v[52:53], v[52:53], v[68:69] neg_lo:[0,1] neg_hi:[0,1]
	v_and_b32_e32 v69, 0xffff0000, v49
	v_lshlrev_b32_e32 v68, 16, v49
	s_add_u32 s12, s14, 0x6d400000
	v_pk_add_f32 v[50:51], v[50:51], v[68:69] neg_lo:[0,1] neg_hi:[0,1]
	s_addc_u32 s13, s15, 0
	v_cvt_pk_bf16_f32 v52, v52, v53
	v_cvt_pk_bf16_f32 v53, v50, v51
	v_cvt_pk_bf16_f32 v50, v54, v55
	s_add_u32 s48, s14, 0x6dc00000
	v_and_b32_e32 v69, 0xffff0000, v50
	v_lshlrev_b32_e32 v68, 16, v50
	v_cvt_pk_bf16_f32 v51, v56, v57
	s_addc_u32 s49, s15, 0
	v_pk_add_f32 v[54:55], v[54:55], v[68:69] neg_lo:[0,1] neg_hi:[0,1]
	v_and_b32_e32 v69, 0xffff0000, v51
	v_lshlrev_b32_e32 v68, 16, v51
	v_readlane_b32 s22, v255, 16
	s_add_u32 s50, s14, 0x6e400000
	v_pk_add_f32 v[56:57], v[56:57], v[68:69] neg_lo:[0,1] neg_hi:[0,1]
	v_readlane_b32 s23, v255, 17
	s_addc_u32 s51, s15, 0
	v_cvt_pk_bf16_f32 v54, v54, v55
	v_cvt_pk_bf16_f32 v55, v56, v57
	v_cvt_pk_bf16_f32 v56, v60, v61
	s_lshl_b64 s[22:23], s[22:23], 2
	v_and_b32_e32 v69, 0xffff0000, v56
	v_lshlrev_b32_e32 v68, 16, v56
	v_cvt_pk_bf16_f32 v57, v58, v59
	s_add_u32 s22, s14, s22
	v_readlane_b32 s34, v255, 8
	v_pk_add_f32 v[60:61], v[60:61], v[68:69] neg_lo:[0,1] neg_hi:[0,1]
	v_and_b32_e32 v69, 0xffff0000, v57
	v_lshlrev_b32_e32 v68, 16, v57
	s_addc_u32 s23, s15, s23
	s_lshl_b32 s92, s34, 10
	v_pk_add_f32 v[58:59], v[58:59], v[68:69] neg_lo:[0,1] neg_hi:[0,1]
	s_lshl_b64 s[30:31], s[92:93], 2
	v_cvt_pk_bf16_f32 v60, v60, v61
	v_cvt_pk_bf16_f32 v61, v58, v59
	v_cvt_pk_bf16_f32 v58, v62, v63
	s_add_u32 s38, s38, s30
	v_and_b32_e32 v70, 63, v72
	v_and_b32_e32 v69, 0xffff0000, v58
	v_lshlrev_b32_e32 v68, 16, v58
	v_cvt_pk_bf16_f32 v59, v64, v65
	s_addc_u32 s39, s39, s31
	v_pk_add_f32 v[62:63], v[62:63], v[68:69] neg_lo:[0,1] neg_hi:[0,1]
	v_and_b32_e32 v69, 0xffff0000, v59
	v_lshlrev_b32_e32 v68, 16, v59
	s_add_u32 s30, s36, s30
	v_lshlrev_b32_e32 v89, 2, v72
	v_readlane_b32 s36, v254, 28
	v_lshlrev_b32_e32 v76, 3, v70
	v_mov_b32_e32 v77, v169
	v_pk_add_f32 v[64:65], v[64:65], v[68:69] neg_lo:[0,1] neg_hi:[0,1]
	s_addc_u32 s31, s37, s31
	v_add_u32_e32 v180, s36, v89
	v_lshl_add_u64 v[68:69], s[14:15], 0, v[76:77]
	s_mov_b64 s[36:37], 0x21400000
	v_lshl_add_u64 v[78:79], v[68:69], 0, s[36:37]
	v_lshlrev_b32_e32 v68, 4, v70
	v_mov_b32_e32 v69, v169
	v_ashrrev_i32_e32 v73, 31, v72
	s_lshl_b32 s92, s34, 5
	v_lshl_add_u64 v[80:81], s[30:31], 0, v[68:69]
	v_lshl_add_u64 v[82:83], s[38:39], 0, v[68:69]
	v_lshl_add_u64 v[68:69], v[72:73], 2, s[22:23]
	s_mov_b64 s[22:23], 0x10000
	s_lshl_b64 s[34:35], s[92:93], 2
	v_lshl_add_u64 v[90:91], v[68:69], 0, s[22:23]
	s_movk_i32 s22, 0x400
	s_add_u32 s40, s42, s34
	v_cmp_gt_i32_e64 s[46:47], s22, v72
	v_readlane_b32 s22, v253, 46
	s_addc_u32 s41, s43, s35
	v_cvt_pk_bf16_f32 v62, v62, v63
	v_lshl_add_u32 v66, v66, 9, s22
	v_readlane_b32 s22, v254, 10
	s_add_u32 s52, s27, s22
	v_readlane_b32 s22, v254, 11
	v_cvt_pk_bf16_f32 v63, v64, v65
	v_lshlrev_b32_e32 v64, 2, v70
	v_mov_b32_e32 v65, v169
	s_movk_i32 s30, 0x810
	s_addc_u32 s53, s29, s22
	v_readlane_b32 s22, v254, 14
	v_lshl_add_u64 v[74:75], s[10:11], 0, v[64:65]
	v_mad_u32_u24 v67, v67, s30, 0
	v_readlane_b32 s30, v252, 3
	v_ashrrev_i32_e32 v77, 5, v72
	v_and_b32_e32 v181, 31, v72
	s_add_u32 s10, s10, s22
	v_readlane_b32 s22, v254, 15
	v_cmp_eq_u32_e64 s[36:37], 0, v70
	v_and_or_b32 v70, v72, 48, s30
	v_lshlrev_b32_e32 v84, 2, v181
	v_mov_b32_e32 v85, v169
	v_readlane_b32 s30, v254, 29
	v_lshlrev_b32_e32 v68, 4, v77
	v_readlane_b32 s23, v254, 30
	s_addc_u32 s11, s11, s22
	v_cmp_gt_i32_e64 s[34:35], 32, v72
	v_lshl_add_u64 v[86:87], s[40:41], 0, v[84:85]
	v_and_b32_e32 v88, 32, v72
	v_cmp_gt_u32_e64 s[38:39], 4, v181
	v_cmp_eq_u32_e64 s[40:41], 0, v181
	v_cmp_eq_u32_e64 s[42:43], 1, v181
	v_cmp_eq_u32_e64 s[44:45], 2, v181
	v_add_u32_e32 v85, s30, v89
	v_and_b32_e32 v73, 3, v72
	v_add3_u32 v182, v68, v84, s23
	v_lshl_add_u64 v[92:93], s[10:11], 0, v[64:65]
	v_add_u32_e32 v183, s23, v89
	v_add_u32_e32 v184, v67, v70
	v_add_u32_e32 v168, v66, v168
	v_readlane_b32 s62, v254, 6
	v_readlane_b32 s54, v252, 5
	v_readlane_b32 s70, v252, 2
	v_readlane_b32 s71, v253, 45
	v_readlane_b32 s72, v254, 7
	v_readlane_b32 s73, v254, 8
	s_movk_i32 s74, 0x4000
	s_mov_b32 s75, 0x8000
	v_readlane_b32 s55, v252, 6
	global_load_dword v246, v[86:87], off
	s_waitcnt vmcnt(0)
	s_branch .LBB0_636

; #define LAS __attribute__((address_space(3)))
; __device__ __forceinline__ unsigned pk2(float lo, float hi) { const f32x2_t v = {lo, hi}; const bf16x2_t b = __builtin_convertvector(v, bf16x2_t); return __builtin_bit_cast(unsigned, b); }
; __device__ __forceinline__ void lds_barrier() { asm volatile("s_waitcnt lgkmcnt(0)" ::: "memory"); __builtin_amdgcn_s_barrier(); asm volatile("" ::: "memory"); }
; __device__ __forceinline__ void p4_ln_router(Frame& F, int l) {
;     ...
;             for (int r = 0; r < 2; ++r) { const int trow = 2 * wave + r;
; #pragma unroll
;                 for (int j = 0; j < 4; ++j) { const f32x4 x = v[r][j]; v2u hi; hi.x = pk2(x.x, x.y); hi.y = pk2(x.z, x.w);
;                     v2u lo; lo.x = pk2(x.x - bflo(hi.x), x.y - bfhi(hi.x)); lo.y = pk2(x.z - bflo(hi.y), x.w - bfhi(hi.y));
;                     *(LAS v2u*)(L + R_HI + trow * R_PITCH + (4 * lane + 256 * j) * 2) = hi; *(LAS v2u*)(L + R_LO + trow * R_PITCH + (4 * lane + 256 * j) * 2) = lo; } }
;             lds_barrier();
;             f32x4 acc[2] = {(f32x4){0.f, 0.f, 0.f, 0.f}, (f32x4){0.f, 0.f, 0.f, 0.f}}, acb[2] = {(f32x4){0.f, 0.f, 0.f, 0.f}, (f32x4){0.f, 0.f, 0.f, 0.f}}, acc3[2] = {(f32x4){0.f, 0.f, 0.f, 0.f}, (f32x4){0.f, 0.f, 0.f, 0.f}};
;             bf16x8_t ah[4], al[4];
; #pragma unroll
;             for (int ks = 0; ks < 4; ++ks) { ah[ks] = *(const LAS bf16x8_t*)(L + R_HI + li * R_PITCH + (128 * wave + 32 * ks + 8 * q4) * 2); al[ks] = *(const LAS bf16x8_t*)(L + R_LO + li * R_PITCH + (128 * wave + 32 * ks + 8 * q4) * 2); }
; #pragma unroll
;             for (int ks = 0; ks < 4; ++ks)
; #pragma unroll
;                 for (int nt = 0; nt < 2; ++nt) { acc[nt] = __builtin_amdgcn_mfma_f32_16x16x32_bf16(ah[ks], whi[ks][nt], acc[nt], 0, 0, 0);
;                     acb[nt] = __builtin_amdgcn_mfma_f32_16x16x32_bf16(al[ks], whi[ks][nt], acb[nt], 0, 0, 0); acc3[nt] = __builtin_amdgcn_mfma_f32_16x16x32_bf16(ah[ks], wlo[ks][nt], acc3[nt], 0, 0, 0); }
; #pragma unroll
;             for (int nt = 0; nt < 2; ++nt) acc[nt] = acc[nt] + (acb[nt] + acc3[nt]);
; #pragma unroll
;             for (int nt = 0; nt < 2; ++nt)
; #pragma unroll
;                 for (int r = 0; r < 4; ++r) *(LAS float*)(L + R_PART + ((wave * 16 + 4 * q4 + r) * 32 + 16 * nt + li) * 4) = acc[nt][r];
;             lds_barrier();
.LBB0_644:
	s_or_b64 exec, exec, s[30:31]
	v_cvt_pk_bf16_f32 v68, v154, v155
	v_cvt_pk_bf16_f32 v69, v152, v153
	v_lshlrev_b32_e32 v70, 16, v68
	v_and_b32_e32 v71, 0xffff0000, v68
	v_lshlrev_b32_e32 v136, 16, v69
	v_and_b32_e32 v137, 0xffff0000, v69
	v_pk_add_f32 v[70:71], v[154:155], v[70:71] neg_lo:[0,1] neg_hi:[0,1]
	v_pk_add_f32 v[136:137], v[152:153], v[136:137] neg_lo:[0,1] neg_hi:[0,1]
	v_cvt_pk_bf16_f32 v70, v70, v71
	v_cvt_pk_bf16_f32 v71, v136, v137
	v_cvt_pk_bf16_f32 v136, v162, v163
	v_cvt_pk_bf16_f32 v137, v160, v161
	v_lshlrev_b32_e32 v138, 16, v136
	v_and_b32_e32 v139, 0xffff0000, v136
	v_lshlrev_b32_e32 v144, 16, v137
	v_and_b32_e32 v145, 0xffff0000, v137
	v_add_u32_e32 v217, s21, v76
	v_pk_add_f32 v[138:139], v[162:163], v[138:139] neg_lo:[0,1] neg_hi:[0,1]
	v_pk_add_f32 v[144:145], v[160:161], v[144:145] neg_lo:[0,1] neg_hi:[0,1]
	v_cvt_pk_bf16_f32 v138, v138, v139
	v_cvt_pk_bf16_f32 v139, v144, v145
	ds_write2st64_b64 v217, v[68:69], v[136:137] offset1:1
	v_add_u32_e32 v218, 0x100, v217
	v_cvt_pk_bf16_f32 v68, v166, v167
	v_cvt_pk_bf16_f32 v69, v164, v165
	ds_write2st64_b64 v218, v[70:71], v[138:139] offset0:64 offset1:65
	v_lshlrev_b32_e32 v70, 16, v68
	v_and_b32_e32 v71, 0xffff0000, v68
	v_lshlrev_b32_e32 v136, 16, v69
	v_and_b32_e32 v137, 0xffff0000, v69
	v_pk_add_f32 v[70:71], v[166:167], v[70:71] neg_lo:[0,1] neg_hi:[0,1]
	v_pk_add_f32 v[136:137], v[164:165], v[136:137] neg_lo:[0,1] neg_hi:[0,1]
	v_cvt_pk_bf16_f32 v70, v70, v71
	v_cvt_pk_bf16_f32 v71, v136, v137
	v_cvt_pk_bf16_f32 v136, v134, v135
	v_cvt_pk_bf16_f32 v137, v132, v133
	v_lshlrev_b32_e32 v138, 16, v136
	v_and_b32_e32 v139, 0xffff0000, v136
	v_pk_add_f32 v[134:135], v[134:135], v[138:139] neg_lo:[0,1] neg_hi:[0,1]
	v_lshlrev_b32_e32 v138, 16, v137
	v_and_b32_e32 v139, 0xffff0000, v137
	v_pk_add_f32 v[132:133], v[132:133], v[138:139] neg_lo:[0,1] neg_hi:[0,1]
	v_cvt_pk_bf16_f32 v134, v134, v135
	v_cvt_pk_bf16_f32 v135, v132, v133
	ds_write2st64_b64 v217, v[68:69], v[136:137] offset0:2 offset1:3
	ds_write2st64_b64 v218, v[70:71], v[134:135] offset0:66 offset1:67
	v_cvt_pk_bf16_f32 v68, v142, v143
	v_cvt_pk_bf16_f32 v69, v140, v141
	v_lshlrev_b32_e32 v70, 16, v68
	v_and_b32_e32 v71, 0xffff0000, v68
	v_lshlrev_b32_e32 v132, 16, v69
	v_and_b32_e32 v133, 0xffff0000, v69
	v_pk_add_f32 v[70:71], v[142:143], v[70:71] neg_lo:[0,1] neg_hi:[0,1]
	v_pk_add_f32 v[132:133], v[140:141], v[132:133] neg_lo:[0,1] neg_hi:[0,1]
	v_cvt_pk_bf16_f32 v70, v70, v71
	v_cvt_pk_bf16_f32 v71, v132, v133
	v_cvt_pk_bf16_f32 v132, v150, v151
	v_cvt_pk_bf16_f32 v133, v148, v149
	v_lshlrev_b32_e32 v134, 16, v132
	v_and_b32_e32 v135, 0xffff0000, v132
	v_lshlrev_b32_e32 v136, 16, v133
	v_and_b32_e32 v137, 0xffff0000, v133
	v_pk_add_f32 v[134:135], v[150:151], v[134:135] neg_lo:[0,1] neg_hi:[0,1]
	v_pk_add_f32 v[136:137], v[148:149], v[136:137] neg_lo:[0,1] neg_hi:[0,1]
	v_add_u32_e32 v219, 16, v217
	v_cvt_pk_bf16_f32 v134, v134, v135
	v_cvt_pk_bf16_f32 v135, v136, v137
	ds_write2st64_b64 v219, v[68:69], v[132:133] offset0:4 offset1:5
	v_add_u32_e32 v220, 0x110, v217
	v_cvt_pk_bf16_f32 v68, v158, v159
	v_cvt_pk_bf16_f32 v69, v156, v157
	ds_write2st64_b64 v220, v[70:71], v[134:135] offset0:68 offset1:69
	v_lshlrev_b32_e32 v70, 16, v68
	v_and_b32_e32 v71, 0xffff0000, v68
	v_lshlrev_b32_e32 v132, 16, v69
	v_and_b32_e32 v133, 0xffff0000, v69
	v_pk_add_f32 v[70:71], v[158:159], v[70:71] neg_lo:[0,1] neg_hi:[0,1]
	v_pk_add_f32 v[132:133], v[156:157], v[132:133] neg_lo:[0,1] neg_hi:[0,1]
	v_cvt_pk_bf16_f32 v70, v70, v71
	v_cvt_pk_bf16_f32 v71, v132, v133
	v_cvt_pk_bf16_f32 v132, v64, v65
	v_cvt_pk_bf16_f32 v133, v66, v67
	v_lshlrev_b32_e32 v134, 16, v132
	v_and_b32_e32 v135, 0xffff0000, v132
	v_pk_add_f32 v[64:65], v[64:65], v[134:135] neg_lo:[0,1] neg_hi:[0,1]
	v_lshlrev_b32_e32 v134, 16, v133
	v_and_b32_e32 v135, 0xffff0000, v133
	v_pk_add_f32 v[66:67], v[66:67], v[134:135] neg_lo:[0,1] neg_hi:[0,1]
	v_cvt_pk_bf16_f32 v64, v64, v65
	v_cvt_pk_bf16_f32 v65, v66, v67
	ds_write2st64_b64 v219, v[68:69], v[132:133] offset0:6 offset1:7
	ds_write2st64_b64 v220, v[70:71], v[64:65] offset0:70 offset1:71
	s_waitcnt lgkmcnt(0)
	s_barrier
	ds_read_b128 v[132:135], v184 offset:33024
	ds_read_b128 v[152:155], v184 offset:33088
	ds_read_b128 v[64:67], v184
	s_waitcnt lgkmcnt(2)
	v_mfma_f32_16x16x32_bf16 v[136:139], v[132:135], v[56:59], 0
	ds_read_b128 v[148:151], v184 offset:64
	v_mfma_f32_16x16x32_bf16 v[132:135], v[132:135], v[48:51], 0
	s_waitcnt lgkmcnt(2)
	v_mfma_f32_16x16x32_bf16 v[136:139], v[152:155], v[40:43], v[136:139]
	v_mfma_f32_16x16x32_bf16 v[132:135], v[152:155], v[32:35], v[132:135]
	ds_read_b128 v[152:155], v184 offset:33152
	s_waitcnt lgkmcnt(2)
	v_mfma_f32_16x16x32_bf16 v[68:71], v[64:67], v[56:59], 0
	v_mfma_f32_16x16x32_bf16 v[140:143], v[64:67], v[60:63], 0
	v_mfma_f32_16x16x32_bf16 v[144:147], v[64:67], v[48:51], 0
	v_mfma_f32_16x16x32_bf16 v[64:67], v[64:67], v[52:55], 0
	s_waitcnt lgkmcnt(0)
	v_mfma_f32_16x16x32_bf16 v[136:139], v[152:155], v[24:27], v[136:139]
	v_mfma_f32_16x16x32_bf16 v[132:135], v[152:155], v[16:19], v[132:135]
	ds_read_b128 v[152:155], v184 offset:33216
	v_mfma_f32_16x16x32_bf16 v[68:71], v[148:151], v[40:43], v[68:71]
	v_mfma_f32_16x16x32_bf16 v[140:143], v[148:151], v[44:47], v[140:143]
	v_mfma_f32_16x16x32_bf16 v[144:147], v[148:151], v[32:35], v[144:147]
	v_mfma_f32_16x16x32_bf16 v[64:67], v[148:151], v[36:39], v[64:67]
	ds_read_b128 v[148:151], v184 offset:128
	s_waitcnt lgkmcnt(0)
	v_mfma_f32_16x16x32_bf16 v[68:71], v[148:151], v[24:27], v[68:71]
	v_mfma_f32_16x16x32_bf16 v[140:143], v[148:151], v[28:31], v[140:143]
	v_mfma_f32_16x16x32_bf16 v[144:147], v[148:151], v[16:19], v[144:147]
	v_mfma_f32_16x16x32_bf16 v[64:67], v[148:151], v[20:23], v[64:67]
	ds_read_b128 v[148:151], v184 offset:192
	v_mfma_f32_16x16x32_bf16 v[136:139], v[152:155], v[8:11], v[136:139]
	s_waitcnt lgkmcnt(0)
	v_mfma_f32_16x16x32_bf16 v[140:143], v[148:151], v[12:15], v[140:143]
	v_mfma_f32_16x16x32_bf16 v[132:135], v[152:155], v[0:3], v[132:135]
	s_nop 6
	v_add_f32_e64 v136, v136, v140
	v_add_f32_e64 v137, v137, v141
	v_pk_add_f32 v[138:139], v[138:139], v[142:143]
	v_mfma_f32_16x16x32_bf16 v[64:67], v[148:151], v[4:7], v[64:67]
	v_mfma_f32_16x16x32_bf16 v[68:71], v[148:151], v[8:11], v[68:71]
	v_mfma_f32_16x16x32_bf16 v[144:147], v[148:151], v[0:3], v[144:147]
	s_nop 5
	v_add_f32_e64 v64, v132, v64
	v_add_f32_e64 v65, v133, v65
	v_pk_add_f32 v[68:69], v[68:69], v[136:137]
	v_pk_add_f32 v[66:67], v[134:135], v[66:67]
	v_pk_add_f32 v[70:71], v[70:71], v[138:139]
	v_pk_add_f32 v[64:65], v[144:145], v[64:65]
	v_pk_add_f32 v[66:67], v[146:147], v[66:67]
	ds_write2_b32 v168, v68, v64 offset1:16
	ds_write2_b32 v168, v69, v65 offset0:32 offset1:48
	ds_write2_b32 v168, v70, v66 offset0:64 offset1:80
	ds_write2_b32 v168, v71, v67 offset0:96 offset1:112
	s_waitcnt lgkmcnt(0)
	s_barrier
; #define LAS __attribute__((address_space(3)))
; template <int CTRL, int RM> __device__ __forceinline__ float dpp_mv(float v) { return __builtin_bit_cast(float, __builtin_amdgcn_update_dpp(__builtin_bit_cast(int, v), __builtin_bit_cast(int, v), CTRL, RM, 0xf, false)); }
; __device__ __forceinline__ float xmax16(float v) { const unsigned u = __builtin_bit_cast(unsigned, v); auto r = __builtin_amdgcn_permlane16_swap(u, u, false, false); return fmaxf(__builtin_bit_cast(float, (unsigned)r[0]), __builtin_bit_cast(float, (unsigned)r[1])); }
; __device__ __forceinline__ void p4_ln_router(Frame& F, int l) {
;     ...
;             { const int row = tid >> 5, e = tid & 31; float val = br[e]; float pw[8];
; #pragma unroll
;                 for (int w = 0; w < 8; ++w) pw[w] = *(const LAS float*)(L + R_PART + ((w * 16 + row) * 32 + e) * 4);
;                 val += ((pw[0] + pw[1]) + (pw[2] + pw[3])) + ((pw[4] + pw[5]) + (pw[6] + pw[7]));
;                 float tv[4]; int te[4];
; #pragma unroll
;                 for (int k = 0; k < 4; ++k) { float mx = val;
;                     mx = fmaxf(mx, dpp_mv<0xb1, 0xf>(mx)); mx = fmaxf(mx, dpp_mv<0x4e, 0xf>(mx)); mx = fmaxf(mx, dpp_mv<0x124, 0xf>(mx)); mx = fmaxf(mx, dpp_mv<0x128, 0xf>(mx)); mx = xmax16(mx);
;                     const unsigned long long bal = __ballot(val == mx); const unsigned hb32 = (unsigned)(bal >> (lane & 32)); const int es = __builtin_ctz(hb32);
;                     tv[k] = mx; te[k] = es; if (e == es) val = -3.0e38f; }
;                 const float e1 = __expf(tv[1] - tv[0]), e2 = __expf(tv[2] - tv[0]), e3 = __expf(tv[3] - tv[0]); const float inv = __builtin_amdgcn_rcpf(1.0f + e1 + e2 + e3);
;                 if (e < 4) { const int ek = e == 0 ? te[0] : e == 1 ? te[1] : e == 2 ? te[2] : te[3];
;                     const float gk = (e == 0 ? 1.0f : e == 1 ? e1 : e == 2 ? e2 : e3) * inv; const int tl = g * 16 + row;
;                     const int lp = __hip_atomic_fetch_add(lcnt + ek, 1, __ATOMIC_RELAXED, __HIP_MEMORY_SCOPE_WORKGROUP);
;                     tokE[tl * 4 + e] = ek; tokP[tl * 4 + e] = lp; tokG[tl * 4 + e] = gk; } }
	v_mov_b32_e32 v132, v246
	v_add_u32_e32 v64, 0, v89
	v_add_u32_e32 v221, 0x10200, v64
	v_add_u32_e32 v222, 0x10a00, v64
	v_add_u32_e32 v223, 0x11200, v64
	v_add_u32_e32 v224, 0x11a00, v64
	v_add_u32_e32 v225, 0x12200, v64
	v_add_u32_e32 v226, 0x12a00, v64
	v_add_u32_e32 v227, 0x13200, v64
	v_add_u32_e32 v228, 0x13a00, v64
	ds_read_b32 v64, v221
	ds_read_b32 v66, v222
	ds_read_b32 v68, v223
	ds_read_b32 v70, v224
	ds_read_b32 v65, v225
	ds_read_b32 v67, v226
	ds_read_b32 v69, v227
	ds_read_b32 v71, v228
	s_waitcnt lgkmcnt(2)
	v_pk_add_f32 v[64:65], v[64:65], v[66:67]
	s_waitcnt lgkmcnt(0)
	v_pk_add_f32 v[66:67], v[68:69], v[70:71]
	s_nop 0
	v_pk_add_f32 v[64:65], v[64:65], v[66:67]
	s_nop 0
	v_add_f32_e32 v64, v64, v65
	s_waitcnt vmcnt(9)
	v_add_f32_e32 v68, v132, v64
	v_mov_b32_e32 v64, v68
	s_nop 1
	v_mov_b32_dpp v64, v64 quad_perm:[1,0,3,2] row_mask:0xf bank_mask:0xf
	v_max_f32_e32 v64, v64, v64
	v_max_f32_e32 v64, v68, v64
	v_mov_b32_e32 v65, v64
	s_nop 1
	v_mov_b32_dpp v65, v65 quad_perm:[2,3,0,1] row_mask:0xf bank_mask:0xf
	v_max_f32_e32 v65, v65, v65
	v_max_f32_e32 v64, v64, v65
	v_mov_b32_e32 v65, v64
	s_nop 1
	v_mov_b32_dpp v65, v65 row_ror:4 row_mask:0xf bank_mask:0xf
	v_max_f32_e32 v65, v65, v65
	v_max_f32_e32 v64, v64, v65
	v_mov_b32_e32 v65, v64
	s_nop 1
	v_mov_b32_dpp v65, v65 row_ror:8 row_mask:0xf bank_mask:0xf
	v_max_f32_e32 v65, v65, v65
	v_max_f32_e32 v64, v64, v65
	v_mov_b32_e32 v65, v64
	s_nop 1
	v_permlane16_swap_b32_e32 v64, v65
	v_max_f32_e32 v65, v65, v65
	v_max_f32_e32 v64, v64, v64
	v_max_f32_e32 v65, v64, v65
	v_cmp_eq_f32_e32 vcc, v68, v65
	s_nop 1
	v_lshrrev_b64 v[66:67], v88, vcc
	v_ffbl_b32_e32 v64, v66
	v_cmp_ne_u32_e32 vcc, v181, v64
	s_nop 1
	v_cndmask_b32_e32 v70, v198, v68, vcc
	v_mov_b32_e32 v66, v70
	s_nop 1
	v_mov_b32_dpp v66, v66 quad_perm:[1,0,3,2] row_mask:0xf bank_mask:0xf
	v_max_f32_e32 v66, v66, v66
	v_max_f32_e32 v66, v70, v66
	v_mov_b32_e32 v67, v66
	s_nop 1
	v_mov_b32_dpp v67, v67 quad_perm:[2,3,0,1] row_mask:0xf bank_mask:0xf
	v_max_f32_e32 v67, v67, v67
	v_max_f32_e32 v66, v66, v67
	v_mov_b32_e32 v67, v66
	s_nop 1
	v_mov_b32_dpp v67, v67 row_ror:4 row_mask:0xf bank_mask:0xf
	v_max_f32_e32 v67, v67, v67
	v_max_f32_e32 v66, v66, v67
	v_mov_b32_e32 v67, v66
	s_nop 1
	v_mov_b32_dpp v67, v67 row_ror:8 row_mask:0xf bank_mask:0xf
	v_max_f32_e32 v67, v67, v67
	v_max_f32_e32 v66, v66, v67
	v_mov_b32_e32 v67, v66
	s_nop 1
	v_permlane16_swap_b32_e32 v66, v67
	v_max_f32_e32 v67, v67, v67
	v_max_f32_e32 v66, v66, v66
	v_max_f32_e32 v67, v66, v67
	v_cmp_eq_f32_e32 vcc, v70, v67
	s_nop 1
	v_lshrrev_b64 v[68:69], v88, vcc
	v_ffbl_b32_e32 v66, v68
	v_cmp_ne_u32_e32 vcc, v181, v66
	s_nop 1
	v_cndmask_b32_e32 v132, v198, v70, vcc
	v_mov_b32_e32 v68, v132
	s_nop 1
	v_mov_b32_dpp v68, v68 quad_perm:[1,0,3,2] row_mask:0xf bank_mask:0xf
	v_max_f32_e32 v68, v68, v68
	v_max_f32_e32 v68, v132, v68
	v_mov_b32_e32 v69, v68
	s_nop 1
	v_mov_b32_dpp v69, v69 quad_perm:[2,3,0,1] row_mask:0xf bank_mask:0xf
	v_max_f32_e32 v69, v69, v69
	v_max_f32_e32 v68, v68, v69
	v_mov_b32_e32 v69, v68
	s_nop 1
	v_mov_b32_dpp v69, v69 row_ror:4 row_mask:0xf bank_mask:0xf
	v_max_f32_e32 v69, v69, v69
	v_max_f32_e32 v68, v68, v69
	v_mov_b32_e32 v69, v68
	s_nop 1
	v_mov_b32_dpp v69, v69 row_ror:8 row_mask:0xf bank_mask:0xf
	v_max_f32_e32 v69, v69, v69
	v_max_f32_e32 v68, v68, v69
	v_mov_b32_e32 v69, v68
	s_nop 1
	v_permlane16_swap_b32_e32 v68, v69
	v_max_f32_e32 v69, v69, v69
	v_max_f32_e32 v68, v68, v68
	v_max_f32_e32 v69, v68, v69
	v_cmp_eq_f32_e32 vcc, v132, v69
	s_nop 1
	v_lshrrev_b64 v[70:71], v88, vcc
	v_ffbl_b32_e32 v68, v70
	v_cmp_ne_u32_e32 vcc, v181, v68
	s_nop 1
	v_cndmask_b32_e32 v71, v198, v132, vcc
	v_mov_b32_e32 v70, v71
	s_nop 1
	v_mov_b32_dpp v70, v70 quad_perm:[1,0,3,2] row_mask:0xf bank_mask:0xf
	v_max_f32_e32 v70, v70, v70
	v_max_f32_e32 v70, v71, v70
	v_mov_b32_e32 v132, v70
	s_nop 1
	v_mov_b32_dpp v132, v132 quad_perm:[2,3,0,1] row_mask:0xf bank_mask:0xf
	v_max_f32_e32 v132, v132, v132
	v_max_f32_e32 v70, v70, v132
	v_mov_b32_e32 v132, v70
	s_nop 1
	v_mov_b32_dpp v132, v132 row_ror:4 row_mask:0xf bank_mask:0xf
	v_max_f32_e32 v132, v132, v132
	v_max_f32_e32 v70, v70, v132
	v_mov_b32_e32 v132, v70
	s_nop 1
	v_mov_b32_dpp v132, v132 row_ror:8 row_mask:0xf bank_mask:0xf
	v_max_f32_e32 v132, v132, v132
	v_max_f32_e32 v70, v70, v132
	v_mov_b32_e32 v132, v70
	s_nop 1
	v_permlane16_swap_b32_e32 v70, v132
	v_max_f32_e32 v132, v132, v132
	v_max_f32_e32 v70, v70, v70
	v_max_f32_e32 v70, v70, v132
	v_cmp_eq_f32_e32 vcc, v71, v70
	s_and_saveexec_b64 s[22:23], s[38:39]
	s_cbranch_execz .LBB0_646
	v_sub_f32_e32 v67, v67, v65
	v_mul_f32_e32 v67, 0x3fb8aa3b, v67
	v_sub_f32_e32 v69, v69, v65
	v_exp_f32_e32 v67, v67
	v_mul_f32_e32 v69, 0x3fb8aa3b, v69
	v_sub_f32_e32 v65, v70, v65
	v_exp_f32_e32 v69, v69
	v_mul_f32_e32 v65, 0x3fb8aa3b, v65
	v_exp_f32_e32 v65, v65
	v_add_f32_e32 v70, 1.0, v67
	v_add_f32_e32 v70, v70, v69
	v_add_f32_e32 v70, v70, v65
	v_rcp_f32_e32 v132, v70
	v_lshrrev_b64 v[70:71], v88, vcc
	v_ffbl_b32_e32 v70, v70
	v_cndmask_b32_e64 v68, v70, v68, s[44:45]
	v_cndmask_b32_e64 v66, v68, v66, s[42:43]
	v_cndmask_b32_e64 v64, v66, v64, s[40:41]
	v_lshl_add_u32 v66, v64, 2, 0
	v_add_u32_e32 v66, 0x23900, v66
	ds_add_rtn_u32 v66, v66, v188
	v_cndmask_b32_e64 v65, v65, v69, s[44:45]
	v_cndmask_b32_e64 v65, v65, v67, s[42:43]
	v_add_u32_e32 v67, 0xffffe000, v185
	v_cndmask_b32_e64 v65, v65, 1.0, s[40:41]
	ds_write_b32 v67, v64
	v_add_u32_e32 v64, 0xfffff000, v185
	v_mul_f32_e32 v65, v132, v65
	s_waitcnt lgkmcnt(1)
	ds_write_b32 v64, v66
	ds_write_b32 v185, v65

; #define LAS __attribute__((address_space(3)))
; __device__ __forceinline__ unsigned pk2(float lo, float hi) { const f32x2_t v = {lo, hi}; const bf16x2_t b = __builtin_convertvector(v, bf16x2_t); return __builtin_bit_cast(unsigned, b); }
; __device__ __forceinline__ void lds_barrier() { asm volatile("s_waitcnt lgkmcnt(0)" ::: "memory"); __builtin_amdgcn_s_barrier(); asm volatile("" ::: "memory"); }
; __device__ __forceinline__ void p4_ln_router(Frame& F, int l) {
;     ...
;             for (int r = 0; r < 2; ++r) { const int trow = 2 * wave + r;
; #pragma unroll
;                 for (int j = 0; j < 4; ++j) { const f32x4 x = v[r][j]; v2u hi; hi.x = pk2(x.x, x.y); hi.y = pk2(x.z, x.w);
;                     v2u lo; lo.x = pk2(x.x - bflo(hi.x), x.y - bfhi(hi.x)); lo.y = pk2(x.z - bflo(hi.y), x.w - bfhi(hi.y));
;                     *(LAS v2u*)(L + R_HI + trow * R_PITCH + (4 * lane + 256 * j) * 2) = hi; *(LAS v2u*)(L + R_LO + trow * R_PITCH + (4 * lane + 256 * j) * 2) = lo; } }
;             lds_barrier();
;             f32x4 acc[2] = {(f32x4){0.f, 0.f, 0.f, 0.f}, (f32x4){0.f, 0.f, 0.f, 0.f}}, acb[2] = {(f32x4){0.f, 0.f, 0.f, 0.f}, (f32x4){0.f, 0.f, 0.f, 0.f}}, acc3[2] = {(f32x4){0.f, 0.f, 0.f, 0.f}, (f32x4){0.f, 0.f, 0.f, 0.f}};
;             bf16x8_t ah[4], al[4];
; #pragma unroll
;             for (int ks = 0; ks < 4; ++ks) { ah[ks] = *(const LAS bf16x8_t*)(L + R_HI + li * R_PITCH + (128 * wave + 32 * ks + 8 * q4) * 2); al[ks] = *(const LAS bf16x8_t*)(L + R_LO + li * R_PITCH + (128 * wave + 32 * ks + 8 * q4) * 2); }
; #pragma unroll
;             for (int ks = 0; ks < 4; ++ks)
; #pragma unroll
;                 for (int nt = 0; nt < 2; ++nt) { acc[nt] = __builtin_amdgcn_mfma_f32_16x16x32_bf16(ah[ks], whi[ks][nt], acc[nt], 0, 0, 0);
;                     acb[nt] = __builtin_amdgcn_mfma_f32_16x16x32_bf16(al[ks], whi[ks][nt], acb[nt], 0, 0, 0); acc3[nt] = __builtin_amdgcn_mfma_f32_16x16x32_bf16(ah[ks], wlo[ks][nt], acc3[nt], 0, 0, 0); }
; #pragma unroll
;             for (int nt = 0; nt < 2; ++nt) acc[nt] = acc[nt] + (acb[nt] + acc3[nt]);
; #pragma unroll
;             for (int nt = 0; nt < 2; ++nt)
; #pragma unroll
;                 for (int r = 0; r < 4; ++r) *(LAS float*)(L + R_PART + ((wave * 16 + 4 * q4 + r) * 32 + 16 * nt + li) * 4) = acc[nt][r];
;             lds_barrier();
.LBB0_650:
	s_or_b64 exec, exec, s[30:31]
	v_cvt_pk_bf16_f32 v68, v154, v155
	v_cvt_pk_bf16_f32 v69, v152, v153
	v_lshlrev_b32_e32 v70, 16, v68
	v_and_b32_e32 v71, 0xffff0000, v68
	v_lshlrev_b32_e32 v114, 16, v69
	v_and_b32_e32 v115, 0xffff0000, v69
	v_pk_add_f32 v[70:71], v[154:155], v[70:71] neg_lo:[0,1] neg_hi:[0,1]
	v_pk_add_f32 v[114:115], v[152:153], v[114:115] neg_lo:[0,1] neg_hi:[0,1]
	v_cvt_pk_bf16_f32 v70, v70, v71
	v_cvt_pk_bf16_f32 v71, v114, v115
	v_cvt_pk_bf16_f32 v114, v162, v163
	v_cvt_pk_bf16_f32 v115, v160, v161
	v_lshlrev_b32_e32 v116, 16, v114
	v_and_b32_e32 v117, 0xffff0000, v114
	v_lshlrev_b32_e32 v124, 16, v115
	v_and_b32_e32 v125, 0xffff0000, v115
	v_pk_add_f32 v[116:117], v[162:163], v[116:117] neg_lo:[0,1] neg_hi:[0,1]
	v_pk_add_f32 v[124:125], v[160:161], v[124:125] neg_lo:[0,1] neg_hi:[0,1]
	v_cvt_pk_bf16_f32 v116, v116, v117
	v_cvt_pk_bf16_f32 v117, v124, v125
	ds_write2st64_b64 v217, v[68:69], v[114:115] offset1:1
	ds_write2st64_b64 v218, v[70:71], v[116:117] offset0:64 offset1:65
	v_cvt_pk_bf16_f32 v68, v166, v167
	v_cvt_pk_bf16_f32 v69, v164, v165
	v_lshlrev_b32_e32 v70, 16, v68
	v_and_b32_e32 v71, 0xffff0000, v68
	v_lshlrev_b32_e32 v114, 16, v69
	v_and_b32_e32 v115, 0xffff0000, v69
	v_pk_add_f32 v[70:71], v[166:167], v[70:71] neg_lo:[0,1] neg_hi:[0,1]
	v_pk_add_f32 v[114:115], v[164:165], v[114:115] neg_lo:[0,1] neg_hi:[0,1]
	v_cvt_pk_bf16_f32 v70, v70, v71
	v_cvt_pk_bf16_f32 v71, v114, v115
	v_cvt_pk_bf16_f32 v114, v126, v127
	v_cvt_pk_bf16_f32 v115, v122, v123
	v_lshlrev_b32_e32 v116, 16, v114
	v_and_b32_e32 v117, 0xffff0000, v114
	v_lshlrev_b32_e32 v124, 16, v115
	v_and_b32_e32 v125, 0xffff0000, v115
	v_pk_add_f32 v[116:117], v[126:127], v[116:117] neg_lo:[0,1] neg_hi:[0,1]
	v_pk_add_f32 v[122:123], v[122:123], v[124:125] neg_lo:[0,1] neg_hi:[0,1]
	v_cvt_pk_bf16_f32 v116, v116, v117
	v_cvt_pk_bf16_f32 v117, v122, v123
	ds_write2st64_b64 v217, v[68:69], v[114:115] offset0:2 offset1:3
	ds_write2st64_b64 v218, v[70:71], v[116:117] offset0:66 offset1:67
	v_cvt_pk_bf16_f32 v68, v120, v121
	v_cvt_pk_bf16_f32 v69, v118, v119
	v_lshlrev_b32_e32 v70, 16, v68
	v_and_b32_e32 v71, 0xffff0000, v68
	v_lshlrev_b32_e32 v114, 16, v69
	v_and_b32_e32 v115, 0xffff0000, v69
	v_pk_add_f32 v[70:71], v[120:121], v[70:71] neg_lo:[0,1] neg_hi:[0,1]
	v_pk_add_f32 v[114:115], v[118:119], v[114:115] neg_lo:[0,1] neg_hi:[0,1]
	v_cvt_pk_bf16_f32 v70, v70, v71
	v_cvt_pk_bf16_f32 v71, v114, v115
	v_cvt_pk_bf16_f32 v114, v150, v151
	v_cvt_pk_bf16_f32 v115, v130, v131
	v_lshlrev_b32_e32 v116, 16, v114
	v_and_b32_e32 v117, 0xffff0000, v114
	v_lshlrev_b32_e32 v118, 16, v115
	v_and_b32_e32 v119, 0xffff0000, v115
	v_pk_add_f32 v[116:117], v[150:151], v[116:117] neg_lo:[0,1] neg_hi:[0,1]
	v_pk_add_f32 v[118:119], v[130:131], v[118:119] neg_lo:[0,1] neg_hi:[0,1]
	v_cvt_pk_bf16_f32 v116, v116, v117
	v_cvt_pk_bf16_f32 v117, v118, v119
	ds_write2st64_b64 v219, v[68:69], v[114:115] offset0:4 offset1:5
	ds_write2st64_b64 v220, v[70:71], v[116:117] offset0:68 offset1:69
	v_cvt_pk_bf16_f32 v68, v158, v159
	v_cvt_pk_bf16_f32 v69, v156, v157
	v_lshlrev_b32_e32 v70, 16, v68
	v_and_b32_e32 v71, 0xffff0000, v68
	v_lshlrev_b32_e32 v114, 16, v69
	v_and_b32_e32 v115, 0xffff0000, v69
	v_pk_add_f32 v[70:71], v[158:159], v[70:71] neg_lo:[0,1] neg_hi:[0,1]
	v_pk_add_f32 v[114:115], v[156:157], v[114:115] neg_lo:[0,1] neg_hi:[0,1]
	v_cvt_pk_bf16_f32 v70, v70, v71
	v_cvt_pk_bf16_f32 v71, v114, v115
	v_cvt_pk_bf16_f32 v114, v64, v65
	v_cvt_pk_bf16_f32 v115, v66, v67
	v_lshlrev_b32_e32 v116, 16, v114
	v_and_b32_e32 v117, 0xffff0000, v114
	v_pk_add_f32 v[64:65], v[64:65], v[116:117] neg_lo:[0,1] neg_hi:[0,1]
	v_lshlrev_b32_e32 v116, 16, v115
	v_and_b32_e32 v117, 0xffff0000, v115
	v_pk_add_f32 v[66:67], v[66:67], v[116:117] neg_lo:[0,1] neg_hi:[0,1]
	v_cvt_pk_bf16_f32 v64, v64, v65
	v_cvt_pk_bf16_f32 v65, v66, v67
	ds_write2st64_b64 v219, v[68:69], v[114:115] offset0:6 offset1:7
	ds_write2st64_b64 v220, v[70:71], v[64:65] offset0:70 offset1:71
	s_waitcnt lgkmcnt(0)
	s_barrier
	ds_read_b128 v[114:117], v184 offset:33024
	ds_read_b128 v[154:157], v184 offset:33088
	ds_read_b128 v[64:67], v184
	s_waitcnt lgkmcnt(2)
	v_mfma_f32_16x16x32_bf16 v[118:121], v[114:117], v[56:59], 0
	ds_read_b128 v[150:153], v184 offset:64
	v_mfma_f32_16x16x32_bf16 v[114:117], v[114:117], v[48:51], 0
	s_waitcnt lgkmcnt(2)
	v_mfma_f32_16x16x32_bf16 v[118:121], v[154:157], v[40:43], v[118:121]
	v_mfma_f32_16x16x32_bf16 v[114:117], v[154:157], v[32:35], v[114:117]
	ds_read_b128 v[154:157], v184 offset:33152
	s_waitcnt lgkmcnt(2)
	v_mfma_f32_16x16x32_bf16 v[68:71], v[64:67], v[56:59], 0
	v_mfma_f32_16x16x32_bf16 v[122:125], v[64:67], v[60:63], 0
	v_mfma_f32_16x16x32_bf16 v[126:129], v[64:67], v[48:51], 0
	v_mfma_f32_16x16x32_bf16 v[64:67], v[64:67], v[52:55], 0
	s_waitcnt lgkmcnt(0)
	v_mfma_f32_16x16x32_bf16 v[118:121], v[154:157], v[24:27], v[118:121]
	v_mfma_f32_16x16x32_bf16 v[114:117], v[154:157], v[16:19], v[114:117]
	ds_read_b128 v[154:157], v184 offset:33216
	v_mfma_f32_16x16x32_bf16 v[68:71], v[150:153], v[40:43], v[68:71]
	v_mfma_f32_16x16x32_bf16 v[122:125], v[150:153], v[44:47], v[122:125]
	v_mfma_f32_16x16x32_bf16 v[126:129], v[150:153], v[32:35], v[126:129]
	v_mfma_f32_16x16x32_bf16 v[64:67], v[150:153], v[36:39], v[64:67]
	ds_read_b128 v[150:153], v184 offset:128
	s_waitcnt lgkmcnt(0)
	v_mfma_f32_16x16x32_bf16 v[68:71], v[150:153], v[24:27], v[68:71]
	v_mfma_f32_16x16x32_bf16 v[122:125], v[150:153], v[28:31], v[122:125]
	v_mfma_f32_16x16x32_bf16 v[126:129], v[150:153], v[16:19], v[126:129]
	v_mfma_f32_16x16x32_bf16 v[64:67], v[150:153], v[20:23], v[64:67]
	ds_read_b128 v[150:153], v184 offset:192
	v_mfma_f32_16x16x32_bf16 v[118:121], v[154:157], v[8:11], v[118:121]
	s_waitcnt lgkmcnt(0)
	v_mfma_f32_16x16x32_bf16 v[122:125], v[150:153], v[12:15], v[122:125]
	v_mfma_f32_16x16x32_bf16 v[114:117], v[154:157], v[0:3], v[114:117]
	s_nop 6
	v_add_f32_e64 v118, v118, v122
	v_add_f32_e64 v119, v119, v123
	v_pk_add_f32 v[120:121], v[120:121], v[124:125]
	v_mfma_f32_16x16x32_bf16 v[64:67], v[150:153], v[4:7], v[64:67]
	v_mfma_f32_16x16x32_bf16 v[68:71], v[150:153], v[8:11], v[68:71]
	v_mfma_f32_16x16x32_bf16 v[126:129], v[150:153], v[0:3], v[126:129]
	s_nop 5
	v_add_f32_e64 v64, v114, v64
	v_add_f32_e64 v65, v115, v65
	v_pk_add_f32 v[68:69], v[68:69], v[118:119]
	v_pk_add_f32 v[66:67], v[116:117], v[66:67]
	v_pk_add_f32 v[70:71], v[70:71], v[120:121]
	v_pk_add_f32 v[64:65], v[126:127], v[64:65]
	v_pk_add_f32 v[66:67], v[128:129], v[66:67]
	ds_write2_b32 v168, v68, v64 offset1:16
	ds_write2_b32 v168, v69, v65 offset0:32 offset1:48
	ds_write2_b32 v168, v70, v66 offset0:64 offset1:80
	ds_write2_b32 v168, v71, v67 offset0:96 offset1:112
	s_waitcnt lgkmcnt(0)
	s_barrier
; #define LAS __attribute__((address_space(3)))
; template <int CTRL, int RM> __device__ __forceinline__ float dpp_mv(float v) { return __builtin_bit_cast(float, __builtin_amdgcn_update_dpp(__builtin_bit_cast(int, v), __builtin_bit_cast(int, v), CTRL, RM, 0xf, false)); }
; __device__ __forceinline__ float xmax16(float v) { const unsigned u = __builtin_bit_cast(unsigned, v); auto r = __builtin_amdgcn_permlane16_swap(u, u, false, false); return fmaxf(__builtin_bit_cast(float, (unsigned)r[0]), __builtin_bit_cast(float, (unsigned)r[1])); }
; __device__ __forceinline__ void p4_ln_router(Frame& F, int l) {
;     ...
;             { const int row = tid >> 5, e = tid & 31; float val = br[e]; float pw[8];
; #pragma unroll
;                 for (int w = 0; w < 8; ++w) pw[w] = *(const LAS float*)(L + R_PART + ((w * 16 + row) * 32 + e) * 4);
;                 val += ((pw[0] + pw[1]) + (pw[2] + pw[3])) + ((pw[4] + pw[5]) + (pw[6] + pw[7]));
;                 float tv[4]; int te[4];
; #pragma unroll
;                 for (int k = 0; k < 4; ++k) { float mx = val;
;                     mx = fmaxf(mx, dpp_mv<0xb1, 0xf>(mx)); mx = fmaxf(mx, dpp_mv<0x4e, 0xf>(mx)); mx = fmaxf(mx, dpp_mv<0x124, 0xf>(mx)); mx = fmaxf(mx, dpp_mv<0x128, 0xf>(mx)); mx = xmax16(mx);
;                     const unsigned long long bal = __ballot(val == mx); const unsigned hb32 = (unsigned)(bal >> (lane & 32)); const int es = __builtin_ctz(hb32);
;                     tv[k] = mx; te[k] = es; if (e == es) val = -3.0e38f; }
;                 const float e1 = __expf(tv[1] - tv[0]), e2 = __expf(tv[2] - tv[0]), e3 = __expf(tv[3] - tv[0]); const float inv = __builtin_amdgcn_rcpf(1.0f + e1 + e2 + e3);
;                 if (e < 4) { const int ek = e == 0 ? te[0] : e == 1 ? te[1] : e == 2 ? te[2] : te[3];
;                     const float gk = (e == 0 ? 1.0f : e == 1 ? e1 : e == 2 ? e2 : e3) * inv; const int tl = g * 16 + row;
;                     const int lp = __hip_atomic_fetch_add(lcnt + ek, 1, __ATOMIC_RELAXED, __HIP_MEMORY_SCOPE_WORKGROUP);
;                     tokE[tl * 4 + e] = ek; tokP[tl * 4 + e] = lp; tokG[tl * 4 + e] = gk; } }
	v_mov_b32_e32 v114, v246
	ds_read_b32 v64, v221
	ds_read_b32 v66, v222
	ds_read_b32 v68, v223
	ds_read_b32 v70, v224
	ds_read_b32 v65, v225
	ds_read_b32 v67, v226
	ds_read_b32 v69, v227
	ds_read_b32 v71, v228
	s_waitcnt lgkmcnt(2)
	v_pk_add_f32 v[64:65], v[64:65], v[66:67]
	s_waitcnt lgkmcnt(0)
	v_pk_add_f32 v[66:67], v[68:69], v[70:71]
	s_nop 0
	v_pk_add_f32 v[64:65], v[64:65], v[66:67]
	s_nop 0
	v_add_f32_e32 v64, v64, v65
	s_waitcnt vmcnt(9)
	v_add_f32_e32 v68, v114, v64
	v_mov_b32_e32 v64, v68
	s_nop 1
	v_mov_b32_dpp v64, v64 quad_perm:[1,0,3,2] row_mask:0xf bank_mask:0xf
	v_max_f32_e32 v64, v64, v64
	v_max_f32_e32 v64, v68, v64
	v_mov_b32_e32 v65, v64
	s_nop 1
	v_mov_b32_dpp v65, v65 quad_perm:[2,3,0,1] row_mask:0xf bank_mask:0xf
	v_max_f32_e32 v65, v65, v65
	v_max_f32_e32 v64, v64, v65
	v_mov_b32_e32 v65, v64
	s_nop 1
	v_mov_b32_dpp v65, v65 row_ror:4 row_mask:0xf bank_mask:0xf
	v_max_f32_e32 v65, v65, v65
	v_max_f32_e32 v64, v64, v65
	v_mov_b32_e32 v65, v64
	s_nop 1
	v_mov_b32_dpp v65, v65 row_ror:8 row_mask:0xf bank_mask:0xf
	v_max_f32_e32 v65, v65, v65
	v_max_f32_e32 v64, v64, v65
	v_mov_b32_e32 v65, v64
	s_nop 1
	v_permlane16_swap_b32_e32 v64, v65
	v_max_f32_e32 v65, v65, v65
	v_max_f32_e32 v64, v64, v64
	v_max_f32_e32 v65, v64, v65
	v_cmp_eq_f32_e32 vcc, v68, v65
	s_nop 1
	v_lshrrev_b64 v[66:67], v88, vcc
	v_ffbl_b32_e32 v64, v66
	v_cmp_ne_u32_e32 vcc, v181, v64
	s_nop 1
	v_cndmask_b32_e32 v70, v198, v68, vcc
	v_mov_b32_e32 v66, v70
	s_nop 1
	v_mov_b32_dpp v66, v66 quad_perm:[1,0,3,2] row_mask:0xf bank_mask:0xf
	v_max_f32_e32 v66, v66, v66
	v_max_f32_e32 v66, v70, v66
	v_mov_b32_e32 v67, v66
	s_nop 1
	v_mov_b32_dpp v67, v67 quad_perm:[2,3,0,1] row_mask:0xf bank_mask:0xf
	v_max_f32_e32 v67, v67, v67
	v_max_f32_e32 v66, v66, v67
	v_mov_b32_e32 v67, v66
	s_nop 1
	v_mov_b32_dpp v67, v67 row_ror:4 row_mask:0xf bank_mask:0xf
	v_max_f32_e32 v67, v67, v67
	v_max_f32_e32 v66, v66, v67
	v_mov_b32_e32 v67, v66
	s_nop 1
	v_mov_b32_dpp v67, v67 row_ror:8 row_mask:0xf bank_mask:0xf
	v_max_f32_e32 v67, v67, v67
	v_max_f32_e32 v66, v66, v67
	v_mov_b32_e32 v67, v66
	s_nop 1
	v_permlane16_swap_b32_e32 v66, v67
	v_max_f32_e32 v67, v67, v67
	v_max_f32_e32 v66, v66, v66
	v_max_f32_e32 v67, v66, v67
	v_cmp_eq_f32_e32 vcc, v70, v67
	s_nop 1
	v_lshrrev_b64 v[68:69], v88, vcc
	v_ffbl_b32_e32 v66, v68
	v_cmp_ne_u32_e32 vcc, v181, v66
	s_nop 1
	v_cndmask_b32_e32 v114, v198, v70, vcc
	v_mov_b32_e32 v68, v114
	s_nop 1
	v_mov_b32_dpp v68, v68 quad_perm:[1,0,3,2] row_mask:0xf bank_mask:0xf
	v_max_f32_e32 v68, v68, v68
	v_max_f32_e32 v68, v114, v68
	v_mov_b32_e32 v69, v68
	s_nop 1
	v_mov_b32_dpp v69, v69 quad_perm:[2,3,0,1] row_mask:0xf bank_mask:0xf
	v_max_f32_e32 v69, v69, v69
	v_max_f32_e32 v68, v68, v69
	v_mov_b32_e32 v69, v68
	s_nop 1
	v_mov_b32_dpp v69, v69 row_ror:4 row_mask:0xf bank_mask:0xf
	v_max_f32_e32 v69, v69, v69
	v_max_f32_e32 v68, v68, v69
	v_mov_b32_e32 v69, v68
	s_nop 1
	v_mov_b32_dpp v69, v69 row_ror:8 row_mask:0xf bank_mask:0xf
	v_max_f32_e32 v69, v69, v69
	v_max_f32_e32 v68, v68, v69
	v_mov_b32_e32 v69, v68
	s_nop 1
	v_permlane16_swap_b32_e32 v68, v69
	v_max_f32_e32 v69, v69, v69
	v_max_f32_e32 v68, v68, v68
	v_max_f32_e32 v69, v68, v69
	v_cmp_eq_f32_e32 vcc, v114, v69
	s_nop 1
	v_lshrrev_b64 v[70:71], v88, vcc
	v_ffbl_b32_e32 v68, v70
	v_cmp_ne_u32_e32 vcc, v181, v68
	s_nop 1
	v_cndmask_b32_e32 v71, v198, v114, vcc
	v_mov_b32_e32 v70, v71
	s_nop 1
	v_mov_b32_dpp v70, v70 quad_perm:[1,0,3,2] row_mask:0xf bank_mask:0xf
	v_max_f32_e32 v70, v70, v70
	v_max_f32_e32 v70, v71, v70
	v_mov_b32_e32 v114, v70
	s_nop 1
	v_mov_b32_dpp v114, v114 quad_perm:[2,3,0,1] row_mask:0xf bank_mask:0xf
	v_max_f32_e32 v114, v114, v114
	v_max_f32_e32 v70, v70, v114
	v_mov_b32_e32 v114, v70
	s_nop 1
	v_mov_b32_dpp v114, v114 row_ror:4 row_mask:0xf bank_mask:0xf
	v_max_f32_e32 v114, v114, v114
	v_max_f32_e32 v70, v70, v114
	v_mov_b32_e32 v114, v70
	s_nop 1
	v_mov_b32_dpp v114, v114 row_ror:8 row_mask:0xf bank_mask:0xf
	v_max_f32_e32 v114, v114, v114
	v_max_f32_e32 v70, v70, v114
	v_mov_b32_e32 v114, v70
	s_nop 1
	v_permlane16_swap_b32_e32 v70, v114
	v_max_f32_e32 v114, v114, v114
	v_max_f32_e32 v70, v70, v70
	v_max_f32_e32 v70, v70, v114
	v_cmp_eq_f32_e32 vcc, v71, v70
	s_and_saveexec_b64 s[10:11], s[38:39]
	s_cbranch_execz .LBB0_639
	v_sub_f32_e32 v67, v67, v65
	v_mul_f32_e32 v67, 0x3fb8aa3b, v67
	v_sub_f32_e32 v69, v69, v65
	v_exp_f32_e32 v67, v67
	v_mul_f32_e32 v69, 0x3fb8aa3b, v69
	v_sub_f32_e32 v65, v70, v65
	v_exp_f32_e32 v69, v69
	v_mul_f32_e32 v65, 0x3fb8aa3b, v65
	v_exp_f32_e32 v65, v65
	v_add_f32_e32 v70, 1.0, v67
	v_add_f32_e32 v70, v70, v69
	v_add_f32_e32 v70, v70, v65
	v_rcp_f32_e32 v114, v70
	v_lshrrev_b64 v[70:71], v88, vcc
	v_ffbl_b32_e32 v70, v70
	v_cndmask_b32_e64 v68, v70, v68, s[44:45]
	v_cndmask_b32_e64 v66, v68, v66, s[42:43]
	v_cndmask_b32_e64 v64, v66, v64, s[40:41]
	v_cndmask_b32_e64 v65, v65, v69, s[44:45]
	v_cndmask_b32_e64 v65, v65, v67, s[42:43]
	v_lshl_add_u32 v67, v64, 2, 0
	v_add_u32_e32 v67, 0x23900, v67
	v_add_u32_e32 v66, s67, v77
	ds_add_rtn_u32 v67, v67, v188
	v_lshl_or_b32 v66, v66, 4, v84
	v_add_u32_e32 v66, 0, v66
	v_add_u32_e32 v68, 0x20900, v66
	v_cndmask_b32_e64 v65, v65, 1.0, s[40:41]
	ds_write_b32 v68, v64
	v_add_u32_e32 v64, 0x21900, v66
	v_mul_f32_e32 v65, v114, v65
	s_waitcnt lgkmcnt(1)
	ds_write_b32 v64, v67
	v_add_u32_e32 v64, 0x22900, v66
	ds_write_b32 v64, v65
	s_branch .LBB0_639
